# v24: v23 with the relocated conversion loop software-pipelined (next tile's loads issued before the LDS transpose of the current one) and non-temporal hints on its streaming loads/stores
# speedup vs baseline: 1.0118x; 1.0118x over previous
.Lx14_begin:
	s_mov_b64 exec, -1
	s_cmp_lg_u32 s33, 0x100
	s_cbranch_scc1 .LBB0_1816
	s_load_dwordx2 s[4:5], s[74:75], 0x130
	s_add_i32 s25, s2, 0xffffff80
	v_lshrrev_b32_e32 v1, 3, v0
	v_and_b32_e32 v2, 7, v0
	v_lshlrev_b32_e32 v3, 13, v1
	v_lshl_add_u32 v3, v2, 5, v3
	v_mul_u32_u24_e32 v4, 0x204, v1
	v_lshl_add_u32 v4, v2, 5, v4
	v_lshrrev_b32_e32 v5, 2, v0
	v_and_b32_e32 v6, 3, v0
	v_mul_u32_u24_e32 v7, 0x2040, v6
	v_lshl_add_u32 v7, v5, 2, v7
	v_lshlrev_b32_e32 v8, 10, v5
	v_lshl_add_u32 v8, v6, 5, v8
	s_waitcnt vmcnt(0) lgkmcnt(0)
	s_add_u32 s4, s4, 0x8000000
	s_addc_u32 s5, s5, 0
	s_add_u32 s6, s54, 0x1400000
	s_addc_u32 s7, s55, 0
	s_lshr_b32 s8, s25, 7
	s_bfe_u32 s9, s25, 0x40003
	s_and_b32 s10, s25, 7
	s_lshl_b32 s11, s8, 22
	s_lshl_b32 s12, s10, 19
	s_add_i32 s11, s11, s12
	s_lshl_b32 s12, s9, 9
	s_add_i32 s11, s11, s12
	s_add_u32 s14, s4, s11
	s_addc_u32 s15, s5, 0
	global_load_dwordx4 v[10:13], v3, s[14:15] nt
	global_load_dwordx4 v[14:17], v3, s[14:15] offset:16 nt
	global_load_dwordx4 v[18:21], v3, s[14:15] offset:256 nt
	global_load_dwordx4 v[22:25], v3, s[14:15] offset:272 nt
.Lxcv_tile:
	s_add_i32 s26, s25, 0x80
	s_cmp_lt_u32 s26, 0x1000
	s_cselect_b32 s26, s26, s25
	s_lshr_b32 s8, s26, 7
	s_bfe_u32 s9, s26, 0x40003
	s_and_b32 s10, s26, 7
	s_lshl_b32 s11, s8, 22
	s_lshl_b32 s12, s10, 19
	s_add_i32 s11, s11, s12
	s_lshl_b32 s12, s9, 9
	s_add_i32 s11, s11, s12
	s_add_u32 s14, s4, s11
	s_addc_u32 s15, s5, 0
	global_load_dwordx4 v[60:63], v3, s[14:15] nt
	global_load_dwordx4 v[64:67], v3, s[14:15] offset:16 nt
	global_load_dwordx4 v[68:71], v3, s[14:15] offset:256 nt
	global_load_dwordx4 v[72:75], v3, s[14:15] offset:272 nt
	s_lshr_b32 s8, s25, 7
	s_bfe_u32 s9, s25, 0x40003
	s_and_b32 s10, s25, 7
	s_lshl_b32 s11, s8, 21
	s_lshl_b32 s12, s9, 17
	s_add_i32 s11, s11, s12
	s_lshl_b32 s12, s10, 7
	s_add_i32 s11, s11, s12
	s_cmp_ge_u32 s8, 25
	s_cselect_b32 s12, 0x1000000, 0
	s_add_i32 s11, s11, s12
	s_add_u32 s16, s6, s11
	s_addc_u32 s17, s7, 0
	s_waitcnt vmcnt(4)
	ds_write2_b32 v4, v10, v11 offset0:0 offset1:1
	ds_write2_b32 v4, v12, v13 offset0:2 offset1:3
	ds_write2_b32 v4, v14, v15 offset0:4 offset1:5
	ds_write2_b32 v4, v16, v17 offset0:6 offset1:7
	ds_write2_b32 v4, v18, v19 offset0:64 offset1:65
	ds_write2_b32 v4, v20, v21 offset0:66 offset1:67
	ds_write2_b32 v4, v22, v23 offset0:68 offset1:69
	ds_write2_b32 v4, v24, v25 offset0:70 offset1:71
	s_waitcnt lgkmcnt(0)
	s_barrier
	ds_read_b32 v30, v7
	ds_read_b32 v31, v7 offset:516
	ds_read_b32 v32, v7 offset:1032
	ds_read_b32 v33, v7 offset:1548
	ds_read_b32 v34, v7 offset:2064
	ds_read_b32 v35, v7 offset:2580
	ds_read_b32 v36, v7 offset:3096
	ds_read_b32 v37, v7 offset:3612
	ds_read_b32 v38, v7 offset:4128
	ds_read_b32 v39, v7 offset:4644
	ds_read_b32 v40, v7 offset:5160
	ds_read_b32 v41, v7 offset:5676
	ds_read_b32 v42, v7 offset:6192
	ds_read_b32 v43, v7 offset:6708
	ds_read_b32 v44, v7 offset:7224
	ds_read_b32 v45, v7 offset:7740
	s_waitcnt lgkmcnt(0)
	v_cvt_pk_bf16_f32 v50, v30, v31
	v_cvt_pk_bf16_f32 v51, v32, v33
	v_cvt_pk_bf16_f32 v52, v34, v35
	v_cvt_pk_bf16_f32 v53, v36, v37
	v_cvt_pk_bf16_f32 v54, v38, v39
	v_cvt_pk_bf16_f32 v55, v40, v41
	v_cvt_pk_bf16_f32 v56, v42, v43
	v_cvt_pk_bf16_f32 v57, v44, v45
	global_store_dwordx4 v8, v[50:53], s[16:17] nt
	global_store_dwordx4 v8, v[54:57], s[16:17] offset:16 nt
	s_barrier
	s_add_i32 s25, s25, 0x80
	s_add_i32 s26, s25, 0x80
	s_cmp_lt_u32 s26, 0x1000
	s_cselect_b32 s26, s26, s25
	s_lshr_b32 s8, s26, 7
	s_bfe_u32 s9, s26, 0x40003
	s_and_b32 s10, s26, 7
	s_lshl_b32 s11, s8, 22
	s_lshl_b32 s12, s10, 19
	s_add_i32 s11, s11, s12
	s_lshl_b32 s12, s9, 9
	s_add_i32 s11, s11, s12
	s_add_u32 s14, s4, s11
	s_addc_u32 s15, s5, 0
	global_load_dwordx4 v[10:13], v3, s[14:15] nt
	global_load_dwordx4 v[14:17], v3, s[14:15] offset:16 nt
	global_load_dwordx4 v[18:21], v3, s[14:15] offset:256 nt
	global_load_dwordx4 v[22:25], v3, s[14:15] offset:272 nt
	s_lshr_b32 s8, s25, 7
	s_bfe_u32 s9, s25, 0x40003
	s_and_b32 s10, s25, 7
	s_lshl_b32 s11, s8, 21
	s_lshl_b32 s12, s9, 17
	s_add_i32 s11, s11, s12
	s_lshl_b32 s12, s10, 7
	s_add_i32 s11, s11, s12
	s_cmp_ge_u32 s8, 25
	s_cselect_b32 s12, 0x1000000, 0
	s_add_i32 s11, s11, s12
	s_add_u32 s16, s6, s11
	s_addc_u32 s17, s7, 0
	s_waitcnt vmcnt(4)
	ds_write2_b32 v4, v60, v61 offset0:0 offset1:1
	ds_write2_b32 v4, v62, v63 offset0:2 offset1:3
	ds_write2_b32 v4, v64, v65 offset0:4 offset1:5
	ds_write2_b32 v4, v66, v67 offset0:6 offset1:7
	ds_write2_b32 v4, v68, v69 offset0:64 offset1:65
	ds_write2_b32 v4, v70, v71 offset0:66 offset1:67
	ds_write2_b32 v4, v72, v73 offset0:68 offset1:69
	ds_write2_b32 v4, v74, v75 offset0:70 offset1:71
	s_waitcnt lgkmcnt(0)
	s_barrier
	ds_read_b32 v30, v7
	ds_read_b32 v31, v7 offset:516
	ds_read_b32 v32, v7 offset:1032
	ds_read_b32 v33, v7 offset:1548
	ds_read_b32 v34, v7 offset:2064
	ds_read_b32 v35, v7 offset:2580
	ds_read_b32 v36, v7 offset:3096
	ds_read_b32 v37, v7 offset:3612
	ds_read_b32 v38, v7 offset:4128
	ds_read_b32 v39, v7 offset:4644
	ds_read_b32 v40, v7 offset:5160
	ds_read_b32 v41, v7 offset:5676
	ds_read_b32 v42, v7 offset:6192
	ds_read_b32 v43, v7 offset:6708
	ds_read_b32 v44, v7 offset:7224
	ds_read_b32 v45, v7 offset:7740
	s_waitcnt lgkmcnt(0)
	v_cvt_pk_bf16_f32 v50, v30, v31
	v_cvt_pk_bf16_f32 v51, v32, v33
	v_cvt_pk_bf16_f32 v52, v34, v35
	v_cvt_pk_bf16_f32 v53, v36, v37
	v_cvt_pk_bf16_f32 v54, v38, v39
	v_cvt_pk_bf16_f32 v55, v40, v41
	v_cvt_pk_bf16_f32 v56, v42, v43
	v_cvt_pk_bf16_f32 v57, v44, v45
	global_store_dwordx4 v8, v[50:53], s[16:17] nt
	global_store_dwordx4 v8, v[54:57], s[16:17] offset:16 nt
	s_barrier
	s_add_i32 s25, s25, 0x80
	s_cmp_lt_u32 s25, 0x1000
	s_cbranch_scc1 .Lxcv_tile
	s_waitcnt vmcnt(0) lgkmcnt(0)
	s_barrier
	v_cmp_eq_u32_e32 vcc, 0, v0
	s_and_saveexec_b64 s[98:99], vcc
	s_cbranch_execz .Lx14_sb_done
	buffer_wbl2 sc1
	s_waitcnt vmcnt(0)
	v_mov_b32_e32 v1, 0xc800
	v_mov_b32_e32 v2, 1
	global_atomic_add v1, v2, s[54:55]
	s_waitcnt vmcnt(0)
	s_mov_b32 s0, 0
